# weight-conversion loops: the two clamped (useless) tail tile loads are exec-masked off, last iteration waits vmcnt(4)
# speedup vs baseline: 1.0021x; 1.0021x over previous
; #define CV_ISSUE(i, buf) do { const ConvJob _j = CV_JOB(i); _Pragma("unroll") for (int _q = 0; _q < 8; ++_q) { const int _row = 2 * (_q * 8 + w) + lrow; const int _g = gp ^ cv_fz(_row); \
;         __builtin_amdgcn_global_load_lds((const unsigned*)(_j.src + (size_t)(_j.k0 + _row) * _j.ld + _j.col0 + _g * 4), (LAS unsigned*)(c.lds + (buf) * 65536 + (_q * 8 + w) * 1024), 16, 0, 2); } } while (0)
; __device__ __forceinline__ void conv_slice(const Ctx& c, int lo0, int n0, int lo1, int n1, int lo2, int n2) {
;     ...
;     CV_ISSUE(0, 0); CV_ISSUE(1, 1);
;     for (int i = 0; i < mine; ++i) {
;         if (i == 0) asm volatile("s_waitcnt vmcnt(8)" ::: "memory"); else if (i == 1) asm volatile("s_waitcnt vmcnt(12)" ::: "memory"); else asm volatile("s_waitcnt vmcnt(16)" ::: "memory");
.LBB0_101:
	s_add_i32 s98, s77, 2
	s_cmp_le_i32 s98, s37
	s_cselect_b64 s[98:99], exec, 0
	s_mov_b64 s[100:101], exec
	s_cmp_lt_i32 s77, s37
	s_cbranch_scc1 .Lcv_nl_0
	s_waitcnt vmcnt(4)

; __device__ __forceinline__ ConvJob conv_job(const Ctx& c, int t) {
;     ...
;     if (i < CV_IN) { const int kb = i % 16, cb = i / 16; j.src = c.in[4]; j.ld = NIN; j.k0 = kb * 128; j.col0 = cb * 128; j.dst = WSP(bf16, WS_WIN); j.dK = 2048; j.drow0 = cb * 128; return j; }
;     i -= CV_IN;
;     if (i < CV_OUT) { const int kb = i % 16, cb = i / 16; j.src = c.in[8]; j.ld = 2048; j.k0 = kb * 128; j.col0 = cb * 128; j.dst = WSP(bf16, WS_WOUT); j.dK = 2048; j.drow0 = cb * 128; return j; }
;     i -= CV_OUT;
;     if (i < CV_GLU) { const int kb = i % 16, cb = i / 16; j.src = c.in[17]; j.ld = 4096; j.k0 = kb * 128; j.col0 = cb * 128; j.dst = WSP(bf16, WS_WGLU); j.dK = 2048; j.drow0 = cb < 16 ? cb * 256 : (cb - 16) * 256 + 128; return j; }
;     i -= CV_GLU;
;     if (i < CV_GU) { const int kb = i % 16, cb = (i / 16) % 8, gu = (i / 128) % 2, le = i / 256;
;         j.src = (gu ? c.in[23] : c.in[22]) + (size_t)le * 2048 * 1024; j.ld = 1024; j.k0 = kb * 128; j.col0 = cb * 128; j.dst = WSP(bf16, WS_WGU) + (size_t)le * 2048 * 2048; j.dK = 2048; j.drow0 = cb * 256 + gu * 128; return j; }
;     i -= CV_GU;
;     { const int kb = i % 8, cb = (i / 8) % 16, le = i / 128;
;         j.src = c.in[24] + (size_t)le * 1024 * 2048; j.ld = 2048; j.k0 = kb * 128; j.col0 = cb * 128; j.dst = WSP(bf16, WS_WD) + (size_t)le * 2048 * 1024; j.dK = 1024; j.drow0 = cb * 128; return j; }
.LBB0_137:
	s_ashr_i32 s15, s14, 31
	s_lshl_b64 s[14:15], s[14:15], 2
	v_add_u32_e32 v5, s0, v9
	s_add_u32 s12, s12, s14
	v_ashrrev_i32_e32 v7, 31, v5
	s_addc_u32 s13, s13, s15
	v_mul_lo_u32 v7, s10, v7
	v_mul_lo_u32 v11, s11, v5
	v_mad_u64_u32 v[66:67], s[14:15], s10, v5, 0
	v_add3_u32 v67, v67, v7, v11
	v_lshl_add_u64 v[66:67], v[66:67], 2, s[12:13]
	v_add_u32_e32 v5, s0, v54
	s_mov_b32 m0, s29
	v_lshl_add_u64 v[66:67], v[66:67], 0, v[2:3]
	v_ashrrev_i32_e32 v7, 31, v5
	s_mov_b64 exec, s[98:99]
	global_load_lds_dwordx4 v[66:67], off nt
	s_mov_b64 exec, s[100:101]
	v_mul_lo_u32 v7, s10, v7
	v_mul_lo_u32 v11, s11, v5
	v_mad_u64_u32 v[66:67], s[14:15], s10, v5, 0
	v_add3_u32 v67, v67, v7, v11
	v_lshl_add_u64 v[66:67], v[66:67], 2, s[12:13]
	v_mov_b32_e32 v5, v3
	v_lshl_add_u64 v[66:67], v[66:67], 0, v[4:5]
	v_add_u32_e32 v5, s0, v55
	s_mov_b32 m0, s30
	v_ashrrev_i32_e32 v7, 31, v5
	s_mov_b64 exec, s[98:99]
	global_load_lds_dwordx4 v[66:67], off nt
	s_mov_b64 exec, s[100:101]
	v_mul_lo_u32 v7, s10, v7
	v_mul_lo_u32 v11, s11, v5
	v_mad_u64_u32 v[66:67], s[14:15], s10, v5, 0
	v_add3_u32 v67, v67, v7, v11
	v_lshl_add_u64 v[66:67], v[66:67], 2, s[12:13]
	v_mov_b32_e32 v7, v3
	v_add_u32_e32 v5, s0, v56
	v_lshl_add_u64 v[66:67], v[66:67], 0, v[6:7]
	s_mov_b32 m0, s31
	v_ashrrev_i32_e32 v7, 31, v5
	s_mov_b64 exec, s[98:99]
	global_load_lds_dwordx4 v[66:67], off nt
	s_mov_b64 exec, s[100:101]
	v_mul_lo_u32 v7, s10, v7
	v_mul_lo_u32 v11, s11, v5
	v_mad_u64_u32 v[66:67], s[14:15], s10, v5, 0
	v_add3_u32 v67, v67, v7, v11
	v_lshl_add_u64 v[66:67], v[66:67], 2, s[12:13]
	v_mov_b32_e32 v11, v3
	v_add_u32_e32 v5, s0, v57
	v_lshl_add_u64 v[66:67], v[66:67], 0, v[10:11]
	s_mov_b32 m0, s33
	v_ashrrev_i32_e32 v7, 31, v5
	s_mov_b64 exec, s[98:99]
	global_load_lds_dwordx4 v[66:67], off nt
	s_mov_b64 exec, s[100:101]
	v_mul_lo_u32 v7, s10, v7
	v_mul_lo_u32 v11, s11, v5
	v_mad_u64_u32 v[66:67], s[14:15], s10, v5, 0
	v_add3_u32 v67, v67, v7, v11
	v_lshl_add_u64 v[66:67], v[66:67], 2, s[12:13]
	v_mov_b32_e32 v13, v3
	v_add_u32_e32 v5, s0, v58
	v_lshl_add_u64 v[66:67], v[66:67], 0, v[12:13]
	s_mov_b32 m0, s97
	v_ashrrev_i32_e32 v7, 31, v5
	s_mov_b64 exec, s[98:99]
	global_load_lds_dwordx4 v[66:67], off nt
	s_mov_b64 exec, s[100:101]
	v_mul_lo_u32 v7, s10, v7
	v_mul_lo_u32 v11, s11, v5
	v_mad_u64_u32 v[66:67], s[14:15], s10, v5, 0
	v_add3_u32 v67, v67, v7, v11
	v_lshl_add_u64 v[66:67], v[66:67], 2, s[12:13]
	v_mov_b32_e32 v15, v3
	v_add_u32_e32 v5, s0, v59
	v_lshl_add_u64 v[66:67], v[66:67], 0, v[14:15]
	s_mov_b32 m0, s79
	v_ashrrev_i32_e32 v7, 31, v5
	s_mov_b64 exec, s[98:99]
	global_load_lds_dwordx4 v[66:67], off nt
	s_mov_b64 exec, s[100:101]
	v_mul_lo_u32 v7, s10, v7
	v_mul_lo_u32 v11, s11, v5
	v_mad_u64_u32 v[66:67], s[14:15], s10, v5, 0
	v_add3_u32 v67, v67, v7, v11
	v_lshl_add_u64 v[66:67], v[66:67], 2, s[12:13]
	v_mov_b32_e32 v17, v3
	v_add_u32_e32 v5, s0, v60
	v_lshl_add_u64 v[66:67], v[66:67], 0, v[16:17]
	s_mov_b32 m0, s19
	v_ashrrev_i32_e32 v7, 31, v5
	s_mov_b64 exec, s[98:99]
	global_load_lds_dwordx4 v[66:67], off nt
	s_mov_b64 exec, s[100:101]
	v_mul_lo_u32 v7, s10, v7
	v_mul_lo_u32 v11, s11, v5
	v_mad_u64_u32 v[66:67], s[10:11], s10, v5, 0
	v_add3_u32 v67, v67, v7, v11
	v_lshl_add_u64 v[66:67], v[66:67], 2, s[12:13]
	v_mov_b32_e32 v19, v3
	v_lshl_add_u64 v[66:67], v[66:67], 0, v[18:19]
	s_add_i32 m0, s18, s27
	s_cmpk_lt_i32 s76, 0x480
	s_mov_b64 exec, s[98:99]
	global_load_lds_dwordx4 v[66:67], off nt
	s_mov_b64 exec, s[100:101]
	s_cselect_b32 s11, 0, 0xfffffb80
	s_add_i32 s11, s11, s76
	s_cmpk_gt_i32 s11, 0x37f
	s_mov_b64 s[16:17], -1
	s_cbranch_scc0 .LBB0_151
	s_cmpk_gt_u32 s11, 0x47f
	s_cbranch_scc0 .LBB0_148
	s_cmpk_gt_u32 s11, 0x67f
	s_cbranch_scc0 .LBB0_145
	s_cmpk_gt_u32 s11, 0x467f
	s_mov_b64 s[12:13], -1
	s_cbranch_scc0 .LBB0_142
	s_add_i32 s0, s11, 0xffffb980
	s_lshr_b32 s0, s0, 7
	s_and_b32 s10, s44, 0x380
	s_and_b32 s18, s42, 0x780
	s_lshl_b64 s[12:13], s[0:1], 22
	v_readlane_b32 s0, v255, 3
	s_add_u32 s14, s0, s12
	v_readlane_b32 s0, v255, 4
	s_addc_u32 s15, s0, s13
	s_mov_b64 s[12:13], 0

; #define CV_ISSUE(i, buf) do { const ConvJob _j = CV_JOB(i); _Pragma("unroll") for (int _q = 0; _q < 8; ++_q) { const int _row = 2 * (_q * 8 + w) + lrow; const int _g = gp ^ cv_fz(_row); \
;         __builtin_amdgcn_global_load_lds((const unsigned*)(_j.src + (size_t)(_j.k0 + _row) * _j.ld + _j.col0 + _g * 4), (LAS unsigned*)(c.lds + (buf) * 65536 + (_q * 8 + w) * 1024), 16, 0, 2); } } while (0)
; __device__ __forceinline__ void conv_slice(const Ctx& c, int lo0, int n0, int lo1, int n1, int lo2, int n2) {
;     ...
;     CV_ISSUE(0, 0); CV_ISSUE(1, 1);
;     for (int i = 0; i < mine; ++i) {
;         if (i == 0) asm volatile("s_waitcnt vmcnt(8)" ::: "memory"); else if (i == 1) asm volatile("s_waitcnt vmcnt(12)" ::: "memory"); else asm volatile("s_waitcnt vmcnt(16)" ::: "memory");
.LBB0_321:
	s_add_i32 s98, s85, 2
	s_cmp_le_i32 s98, s70
	s_cselect_b64 s[98:99], exec, 0
	s_mov_b64 s[100:101], exec
	s_cmp_lt_i32 s85, s70
	s_cbranch_scc1 .Lcv_nl_1
	s_waitcnt vmcnt(4)

; __device__ __forceinline__ ConvJob conv_job(const Ctx& c, int t) {
;     ...
;     if (i < CV_IN) { const int kb = i % 16, cb = i / 16; j.src = c.in[4]; j.ld = NIN; j.k0 = kb * 128; j.col0 = cb * 128; j.dst = WSP(bf16, WS_WIN); j.dK = 2048; j.drow0 = cb * 128; return j; }
;     i -= CV_IN;
;     if (i < CV_OUT) { const int kb = i % 16, cb = i / 16; j.src = c.in[8]; j.ld = 2048; j.k0 = kb * 128; j.col0 = cb * 128; j.dst = WSP(bf16, WS_WOUT); j.dK = 2048; j.drow0 = cb * 128; return j; }
;     i -= CV_OUT;
;     if (i < CV_GLU) { const int kb = i % 16, cb = i / 16; j.src = c.in[17]; j.ld = 4096; j.k0 = kb * 128; j.col0 = cb * 128; j.dst = WSP(bf16, WS_WGLU); j.dK = 2048; j.drow0 = cb < 16 ? cb * 256 : (cb - 16) * 256 + 128; return j; }
;     i -= CV_GLU;
;     if (i < CV_GU) { const int kb = i % 16, cb = (i / 16) % 8, gu = (i / 128) % 2, le = i / 256;
;         j.src = (gu ? c.in[23] : c.in[22]) + (size_t)le * 2048 * 1024; j.ld = 1024; j.k0 = kb * 128; j.col0 = cb * 128; j.dst = WSP(bf16, WS_WGU) + (size_t)le * 2048 * 2048; j.dK = 2048; j.drow0 = cb * 256 + gu * 128; return j; }
;     i -= CV_GU;
;     { const int kb = i % 8, cb = (i / 8) % 16, le = i / 128;
;         j.src = c.in[24] + (size_t)le * 1024 * 2048; j.ld = 2048; j.k0 = kb * 128; j.col0 = cb * 128; j.dst = WSP(bf16, WS_WD) + (size_t)le * 2048 * 1024; j.dK = 1024; j.drow0 = cb * 128; return j; }
.LBB0_357:
	s_ashr_i32 s21, s20, 31
	s_lshl_b64 s[20:21], s[20:21], 2
	v_add_u32_e32 v3, s10, v50
	s_add_u32 s18, s18, s20
	v_ashrrev_i32_e32 v5, 31, v3
	s_addc_u32 s19, s19, s21
	v_mul_lo_u32 v5, s16, v5
	v_mul_lo_u32 v7, s17, v3
	v_mad_u64_u32 v[64:65], s[20:21], s16, v3, 0
	v_add3_u32 v65, v65, v5, v7
	v_lshl_add_u64 v[64:65], v[64:65], 2, s[18:19]
	v_add_u32_e32 v3, s10, v51
	s_mov_b32 m0, s1
	v_lshl_add_u64 v[64:65], v[64:65], 0, v[0:1]
	v_ashrrev_i32_e32 v5, 31, v3
	s_mov_b64 exec, s[98:99]
	global_load_lds_dwordx4 v[64:65], off nt
	s_mov_b64 exec, s[100:101]
	v_mul_lo_u32 v5, s16, v5
	v_mul_lo_u32 v7, s17, v3
	v_mad_u64_u32 v[64:65], s[20:21], s16, v3, 0
	v_add3_u32 v65, v65, v5, v7
	v_lshl_add_u64 v[64:65], v[64:65], 2, s[18:19]
	v_mov_b32_e32 v3, v1
	v_lshl_add_u64 v[64:65], v[64:65], 0, v[2:3]
	v_add_u32_e32 v3, s10, v52
	s_mov_b32 m0, s60
	v_ashrrev_i32_e32 v5, 31, v3
	s_mov_b64 exec, s[98:99]
	global_load_lds_dwordx4 v[64:65], off nt
	s_mov_b64 exec, s[100:101]
	v_mul_lo_u32 v5, s16, v5
	v_mul_lo_u32 v7, s17, v3
	v_mad_u64_u32 v[64:65], s[20:21], s16, v3, 0
	v_add3_u32 v65, v65, v5, v7
	v_lshl_add_u64 v[64:65], v[64:65], 2, s[18:19]
	v_mov_b32_e32 v5, v1
	v_add_u32_e32 v3, s10, v53
	v_lshl_add_u64 v[64:65], v[64:65], 0, v[4:5]
	s_mov_b32 m0, s61
	v_ashrrev_i32_e32 v5, 31, v3
	s_mov_b64 exec, s[98:99]
	global_load_lds_dwordx4 v[64:65], off nt
	s_mov_b64 exec, s[100:101]
	v_mul_lo_u32 v5, s16, v5
	v_mul_lo_u32 v7, s17, v3
	v_mad_u64_u32 v[64:65], s[20:21], s16, v3, 0
	v_add3_u32 v65, v65, v5, v7
	v_lshl_add_u64 v[64:65], v[64:65], 2, s[18:19]
	v_mov_b32_e32 v7, v1
	v_add_u32_e32 v3, s10, v54
	v_lshl_add_u64 v[64:65], v[64:65], 0, v[6:7]
	s_mov_b32 m0, s66
	v_ashrrev_i32_e32 v5, 31, v3
	s_mov_b64 exec, s[98:99]
	global_load_lds_dwordx4 v[64:65], off nt
	s_mov_b64 exec, s[100:101]
	v_mul_lo_u32 v5, s16, v5
	v_mul_lo_u32 v7, s17, v3
	v_mad_u64_u32 v[64:65], s[20:21], s16, v3, 0
	v_add3_u32 v65, v65, v5, v7
	v_lshl_add_u64 v[64:65], v[64:65], 2, s[18:19]
	v_mov_b32_e32 v9, v1
	v_add_u32_e32 v3, s10, v55
	v_lshl_add_u64 v[64:65], v[64:65], 0, v[8:9]
	s_mov_b32 m0, s97
	v_ashrrev_i32_e32 v5, 31, v3
	s_mov_b64 exec, s[98:99]
	global_load_lds_dwordx4 v[64:65], off nt
	s_mov_b64 exec, s[100:101]
	v_mul_lo_u32 v5, s16, v5
	v_mul_lo_u32 v7, s17, v3
	v_mad_u64_u32 v[64:65], s[20:21], s16, v3, 0
	v_add3_u32 v65, v65, v5, v7
	v_lshl_add_u64 v[64:65], v[64:65], 2, s[18:19]
	v_mov_b32_e32 v11, v1
	v_add_u32_e32 v3, s10, v56
	v_lshl_add_u64 v[64:65], v[64:65], 0, v[10:11]
	s_mov_b32 m0, s89
	v_ashrrev_i32_e32 v5, 31, v3
	s_mov_b64 exec, s[98:99]
	global_load_lds_dwordx4 v[64:65], off nt
	s_mov_b64 exec, s[100:101]
	v_mul_lo_u32 v5, s16, v5
	v_mul_lo_u32 v7, s17, v3
	v_mad_u64_u32 v[64:65], s[20:21], s16, v3, 0
	v_add3_u32 v65, v65, v5, v7
	v_lshl_add_u64 v[64:65], v[64:65], 2, s[18:19]
	v_mov_b32_e32 v13, v1
	v_add_u32_e32 v3, s10, v57
	v_lshl_add_u64 v[64:65], v[64:65], 0, v[12:13]
	s_mov_b32 m0, s25
	v_ashrrev_i32_e32 v5, 31, v3
	s_mov_b64 exec, s[98:99]
	global_load_lds_dwordx4 v[64:65], off nt
	s_mov_b64 exec, s[100:101]
	v_mul_lo_u32 v5, s16, v5
	v_mul_lo_u32 v7, s17, v3
	v_mad_u64_u32 v[64:65], s[16:17], s16, v3, 0
	v_add3_u32 v65, v65, v5, v7
	v_lshl_add_u64 v[64:65], v[64:65], 2, s[18:19]
	v_mov_b32_e32 v15, v1
	v_lshl_add_u64 v[64:65], v[64:65], 0, v[14:15]
	s_add_i32 m0, s24, s43
	s_cmpk_lt_i32 s84, 0x2200
	s_mov_b64 exec, s[98:99]
	global_load_lds_dwordx4 v[64:65], off nt
	s_mov_b64 exec, s[100:101]
	s_cselect_b32 s17, s79, 0xffffde00
	s_add_i32 s17, s17, s84
	s_cmpk_gt_i32 s17, 0x37f
	s_mov_b64 s[22:23], -1
	s_cbranch_scc0 .LBB0_371
	s_cmpk_gt_u32 s17, 0x47f
	s_cbranch_scc0 .LBB0_368
	s_cmpk_gt_u32 s17, 0x67f
	s_cbranch_scc0 .LBB0_365
	s_cmpk_gt_u32 s17, 0x467f
	s_mov_b64 s[18:19], -1
	s_cbranch_scc0 .LBB0_362
	s_add_i32 s1, s17, 0xffffb980
	s_lshr_b32 s10, s1, 7
	s_and_b32 s16, s77, 0x380
	s_and_b32 s24, s75, 0x780
	s_lshl_b64 s[18:19], s[10:11], 22
	s_add_u32 s20, s71, s18
	s_addc_u32 s21, s72, s19
	s_mov_b64 s[18:19], 0

; #define CV_ISSUE(i, buf) do { const ConvJob _j = CV_JOB(i); _Pragma("unroll") for (int _q = 0; _q < 8; ++_q) { const int _row = 2 * (_q * 8 + w) + lrow; const int _g = gp ^ cv_fz(_row); \
;         __builtin_amdgcn_global_load_lds((const unsigned*)(_j.src + (size_t)(_j.k0 + _row) * _j.ld + _j.col0 + _g * 4), (LAS unsigned*)(c.lds + (buf) * 65536 + (_q * 8 + w) * 1024), 16, 0, 2); } } while (0)
; __device__ __forceinline__ void conv_slice(const Ctx& c, int lo0, int n0, int lo1, int n1, int lo2, int n2) {
;     ...
;     CV_ISSUE(0, 0); CV_ISSUE(1, 1);
;     for (int i = 0; i < mine; ++i) {
;         if (i == 0) asm volatile("s_waitcnt vmcnt(8)" ::: "memory"); else if (i == 1) asm volatile("s_waitcnt vmcnt(12)" ::: "memory"); else asm volatile("s_waitcnt vmcnt(16)" ::: "memory");
.LBB0_906:
	s_add_i32 s98, s84, 2
	s_cmp_le_i32 s98, s11
	s_cselect_b64 s[98:99], exec, 0
	s_mov_b64 s[100:101], exec
	s_cmp_lt_i32 s84, s11
	s_cbranch_scc1 .Lcv_nl_2
	s_waitcnt vmcnt(4)

; __device__ __forceinline__ ConvJob conv_job(const Ctx& c, int t) {
;     ...
;     if (i < CV_IN) { const int kb = i % 16, cb = i / 16; j.src = c.in[4]; j.ld = NIN; j.k0 = kb * 128; j.col0 = cb * 128; j.dst = WSP(bf16, WS_WIN); j.dK = 2048; j.drow0 = cb * 128; return j; }
;     i -= CV_IN;
;     if (i < CV_OUT) { const int kb = i % 16, cb = i / 16; j.src = c.in[8]; j.ld = 2048; j.k0 = kb * 128; j.col0 = cb * 128; j.dst = WSP(bf16, WS_WOUT); j.dK = 2048; j.drow0 = cb * 128; return j; }
;     i -= CV_OUT;
;     if (i < CV_GLU) { const int kb = i % 16, cb = i / 16; j.src = c.in[17]; j.ld = 4096; j.k0 = kb * 128; j.col0 = cb * 128; j.dst = WSP(bf16, WS_WGLU); j.dK = 2048; j.drow0 = cb < 16 ? cb * 256 : (cb - 16) * 256 + 128; return j; }
;     i -= CV_GLU;
;     if (i < CV_GU) { const int kb = i % 16, cb = (i / 16) % 8, gu = (i / 128) % 2, le = i / 256;
;         j.src = (gu ? c.in[23] : c.in[22]) + (size_t)le * 2048 * 1024; j.ld = 1024; j.k0 = kb * 128; j.col0 = cb * 128; j.dst = WSP(bf16, WS_WGU) + (size_t)le * 2048 * 2048; j.dK = 2048; j.drow0 = cb * 256 + gu * 128; return j; }
;     i -= CV_GU;
;     { const int kb = i % 8, cb = (i / 8) % 16, le = i / 128;
;         j.src = c.in[24] + (size_t)le * 1024 * 2048; j.ld = 2048; j.k0 = kb * 128; j.col0 = cb * 128; j.dst = WSP(bf16, WS_WD) + (size_t)le * 2048 * 1024; j.dK = 1024; j.drow0 = cb * 128; return j; }
.LBB0_942:
	s_ashr_i32 s25, s24, 31
	s_lshl_b64 s[24:25], s[24:25], 2
	v_add_u32_e32 v3, s0, v50
	s_add_u32 s22, s22, s24
	v_ashrrev_i32_e32 v5, 31, v3
	s_addc_u32 s23, s23, s25
	v_mul_lo_u32 v5, s20, v5
	v_mul_lo_u32 v7, s21, v3
	v_mad_u64_u32 v[64:65], s[24:25], s20, v3, 0
	v_add3_u32 v65, v65, v5, v7
	v_lshl_add_u64 v[64:65], v[64:65], 2, s[22:23]
	v_add_u32_e32 v3, s0, v51
	s_mov_b32 m0, s69
	v_lshl_add_u64 v[64:65], v[64:65], 0, v[0:1]
	v_ashrrev_i32_e32 v5, 31, v3
	s_mov_b64 exec, s[98:99]
	global_load_lds_dwordx4 v[64:65], off nt
	s_mov_b64 exec, s[100:101]
	v_mul_lo_u32 v5, s20, v5
	v_mul_lo_u32 v7, s21, v3
	v_mad_u64_u32 v[64:65], s[24:25], s20, v3, 0
	v_add3_u32 v65, v65, v5, v7
	v_lshl_add_u64 v[64:65], v[64:65], 2, s[22:23]
	v_mov_b32_e32 v3, v1
	v_lshl_add_u64 v[64:65], v[64:65], 0, v[2:3]
	v_add_u32_e32 v3, s0, v52
	s_mov_b32 m0, s70
	v_ashrrev_i32_e32 v5, 31, v3
	s_mov_b64 exec, s[98:99]
	global_load_lds_dwordx4 v[64:65], off nt
	s_mov_b64 exec, s[100:101]
	v_mul_lo_u32 v5, s20, v5
	v_mul_lo_u32 v7, s21, v3
	v_mad_u64_u32 v[64:65], s[24:25], s20, v3, 0
	v_add3_u32 v65, v65, v5, v7
	v_lshl_add_u64 v[64:65], v[64:65], 2, s[22:23]
	v_mov_b32_e32 v5, v1
	v_add_u32_e32 v3, s0, v53
	v_lshl_add_u64 v[64:65], v[64:65], 0, v[4:5]
	s_mov_b32 m0, s97
	v_ashrrev_i32_e32 v5, 31, v3
	s_mov_b64 exec, s[98:99]
	global_load_lds_dwordx4 v[64:65], off nt
	s_mov_b64 exec, s[100:101]
	v_mul_lo_u32 v5, s20, v5
	v_mul_lo_u32 v7, s21, v3
	v_mad_u64_u32 v[64:65], s[24:25], s20, v3, 0
	v_add3_u32 v65, v65, v5, v7
	v_lshl_add_u64 v[64:65], v[64:65], 2, s[22:23]
	v_mov_b32_e32 v7, v1
	v_add_u32_e32 v3, s0, v54
	v_lshl_add_u64 v[64:65], v[64:65], 0, v[6:7]
	s_mov_b32 m0, s89
	v_ashrrev_i32_e32 v5, 31, v3
	s_mov_b64 exec, s[98:99]
	global_load_lds_dwordx4 v[64:65], off nt
	s_mov_b64 exec, s[100:101]
	v_mul_lo_u32 v5, s20, v5
	v_mul_lo_u32 v7, s21, v3
	v_mad_u64_u32 v[64:65], s[24:25], s20, v3, 0
	v_add3_u32 v65, v65, v5, v7
	v_lshl_add_u64 v[64:65], v[64:65], 2, s[22:23]
	v_mov_b32_e32 v9, v1
	v_add_u32_e32 v3, s0, v55
	v_lshl_add_u64 v[64:65], v[64:65], 0, v[8:9]
	s_mov_b32 m0, s88
	v_ashrrev_i32_e32 v5, 31, v3
	s_mov_b64 exec, s[98:99]
	global_load_lds_dwordx4 v[64:65], off nt
	s_mov_b64 exec, s[100:101]
	v_mul_lo_u32 v5, s20, v5
	v_mul_lo_u32 v7, s21, v3
	v_mad_u64_u32 v[64:65], s[24:25], s20, v3, 0
	v_add3_u32 v65, v65, v5, v7
	v_lshl_add_u64 v[64:65], v[64:65], 2, s[22:23]
	v_mov_b32_e32 v11, v1
	v_add_u32_e32 v3, s0, v56
	v_lshl_add_u64 v[64:65], v[64:65], 0, v[10:11]
	s_mov_b32 m0, s85
	v_ashrrev_i32_e32 v5, 31, v3
	s_mov_b64 exec, s[98:99]
	global_load_lds_dwordx4 v[64:65], off nt
	s_mov_b64 exec, s[100:101]
	v_mul_lo_u32 v5, s20, v5
	v_mul_lo_u32 v7, s21, v3
	v_mad_u64_u32 v[64:65], s[24:25], s20, v3, 0
	v_add3_u32 v65, v65, v5, v7
	v_lshl_add_u64 v[64:65], v[64:65], 2, s[22:23]
	v_mov_b32_e32 v13, v1
	v_add_u32_e32 v3, s0, v57
	v_lshl_add_u64 v[64:65], v[64:65], 0, v[12:13]
	s_mov_b32 m0, s29
	v_ashrrev_i32_e32 v5, 31, v3
	s_mov_b64 exec, s[98:99]
	global_load_lds_dwordx4 v[64:65], off nt
	s_mov_b64 exec, s[100:101]
	v_mul_lo_u32 v5, s20, v5
	v_mul_lo_u32 v7, s21, v3
	v_mad_u64_u32 v[64:65], s[20:21], s20, v3, 0
	v_add3_u32 v65, v65, v5, v7
	v_lshl_add_u64 v[64:65], v[64:65], 2, s[22:23]
	v_mov_b32_e32 v15, v1
	v_lshl_add_u64 v[64:65], v[64:65], 0, v[14:15]
	s_add_i32 m0, s28, s80
	s_cmp_ge_i32 s36, s33
	s_mov_b64 exec, s[98:99]
	global_load_lds_dwordx4 v[64:65], off nt
	s_mov_b64 exec, s[100:101]
	s_cselect_b32 s21, s38, 0x4680
	s_add_i32 s21, s21, s36
	s_cmpk_gt_i32 s21, 0x37f
	s_mov_b64 s[26:27], -1
	s_cbranch_scc0 .LBB0_956
	s_cmpk_gt_u32 s21, 0x47f
	s_cbranch_scc0 .LBB0_953
	s_cmpk_gt_u32 s21, 0x67f
	s_cbranch_scc0 .LBB0_950
	s_cmpk_gt_u32 s21, 0x467f
	s_mov_b64 s[22:23], -1
	s_cbranch_scc0 .LBB0_947
	s_add_i32 s0, s21, 0xffffb980
	s_lshr_b32 s0, s0, 7
	s_lshl_b32 s20, s21, 7
	s_lshl_b32 s22, s21, 4
	s_and_b32 s20, s20, 0x380
	s_and_b32 s28, s22, 0x780
	s_lshl_b64 s[22:23], s[0:1], 22
	s_add_u32 s24, s81, s22
	s_addc_u32 s25, s82, s23
	s_mov_b64 s[22:23], 0

; #define CV_ISSUE(i, buf) do { const ConvJob _j = CV_JOB(i); _Pragma("unroll") for (int _q = 0; _q < 8; ++_q) { const int _row = 2 * (_q * 8 + w) + lrow; const int _g = gp ^ cv_fz(_row); \
;         __builtin_amdgcn_global_load_lds((const unsigned*)(_j.src + (size_t)(_j.k0 + _row) * _j.ld + _j.col0 + _g * 4), (LAS unsigned*)(c.lds + (buf) * 65536 + (_q * 8 + w) * 1024), 16, 0, 2); } } while (0)
; __device__ __forceinline__ void conv_slice(const Ctx& c, int lo0, int n0, int lo1, int n1, int lo2, int n2) {
;     ...
;     CV_ISSUE(0, 0); CV_ISSUE(1, 1);
;     for (int i = 0; i < mine; ++i) {
;         if (i == 0) asm volatile("s_waitcnt vmcnt(8)" ::: "memory"); else if (i == 1) asm volatile("s_waitcnt vmcnt(12)" ::: "memory"); else asm volatile("s_waitcnt vmcnt(16)" ::: "memory");
.LBB0_1008:
	s_add_i32 s98, s76, 2
	s_cmp_le_i32 s98, s72
	s_cselect_b64 s[98:99], exec, 0
	s_mov_b64 s[100:101], exec
	s_cmp_lt_i32 s76, s72
	s_cbranch_scc1 .Lcv_nl_3
	s_waitcnt vmcnt(4)

; __device__ __forceinline__ ConvJob conv_job(const Ctx& c, int t) {
;     ...
;     if (i < CV_IN) { const int kb = i % 16, cb = i / 16; j.src = c.in[4]; j.ld = NIN; j.k0 = kb * 128; j.col0 = cb * 128; j.dst = WSP(bf16, WS_WIN); j.dK = 2048; j.drow0 = cb * 128; return j; }
;     i -= CV_IN;
;     if (i < CV_OUT) { const int kb = i % 16, cb = i / 16; j.src = c.in[8]; j.ld = 2048; j.k0 = kb * 128; j.col0 = cb * 128; j.dst = WSP(bf16, WS_WOUT); j.dK = 2048; j.drow0 = cb * 128; return j; }
;     i -= CV_OUT;
;     if (i < CV_GLU) { const int kb = i % 16, cb = i / 16; j.src = c.in[17]; j.ld = 4096; j.k0 = kb * 128; j.col0 = cb * 128; j.dst = WSP(bf16, WS_WGLU); j.dK = 2048; j.drow0 = cb < 16 ? cb * 256 : (cb - 16) * 256 + 128; return j; }
;     i -= CV_GLU;
;     if (i < CV_GU) { const int kb = i % 16, cb = (i / 16) % 8, gu = (i / 128) % 2, le = i / 256;
;         j.src = (gu ? c.in[23] : c.in[22]) + (size_t)le * 2048 * 1024; j.ld = 1024; j.k0 = kb * 128; j.col0 = cb * 128; j.dst = WSP(bf16, WS_WGU) + (size_t)le * 2048 * 2048; j.dK = 2048; j.drow0 = cb * 256 + gu * 128; return j; }
;     i -= CV_GU;
;     { const int kb = i % 8, cb = (i / 8) % 16, le = i / 128;
;         j.src = c.in[24] + (size_t)le * 1024 * 2048; j.ld = 2048; j.k0 = kb * 128; j.col0 = cb * 128; j.dst = WSP(bf16, WS_WD) + (size_t)le * 2048 * 1024; j.dK = 1024; j.drow0 = cb * 128; return j; }
.LBB0_1044:
	s_ashr_i32 s25, s24, 31
	s_lshl_b64 s[24:25], s[24:25], 2
	v_add_u32_e32 v3, s0, v50
	s_add_u32 s22, s22, s24
	v_ashrrev_i32_e32 v5, 31, v3
	s_addc_u32 s23, s23, s25
	v_mul_lo_u32 v5, s20, v5
	v_mul_lo_u32 v7, s21, v3
	v_mad_u64_u32 v[64:65], s[24:25], s20, v3, 0
	v_add3_u32 v65, v65, v5, v7
	v_lshl_add_u64 v[64:65], v[64:65], 2, s[22:23]
	v_add_u32_e32 v3, s0, v51
	s_mov_b32 m0, s49
	v_lshl_add_u64 v[64:65], v[64:65], 0, v[0:1]
	v_ashrrev_i32_e32 v5, 31, v3
	s_mov_b64 exec, s[98:99]
	global_load_lds_dwordx4 v[64:65], off nt
	s_mov_b64 exec, s[100:101]
	v_mul_lo_u32 v5, s20, v5
	v_mul_lo_u32 v7, s21, v3
	v_mad_u64_u32 v[64:65], s[24:25], s20, v3, 0
	v_add3_u32 v65, v65, v5, v7
	v_lshl_add_u64 v[64:65], v[64:65], 2, s[22:23]
	v_mov_b32_e32 v3, v1
	v_lshl_add_u64 v[64:65], v[64:65], 0, v[2:3]
	v_add_u32_e32 v3, s0, v52
	s_mov_b32 m0, s48
	v_ashrrev_i32_e32 v5, 31, v3
	s_mov_b64 exec, s[98:99]
	global_load_lds_dwordx4 v[64:65], off nt
	s_mov_b64 exec, s[100:101]
	v_mul_lo_u32 v5, s20, v5
	v_mul_lo_u32 v7, s21, v3
	v_mad_u64_u32 v[64:65], s[24:25], s20, v3, 0
	v_add3_u32 v65, v65, v5, v7
	v_lshl_add_u64 v[64:65], v[64:65], 2, s[22:23]
	v_mov_b32_e32 v5, v1
	v_add_u32_e32 v3, s0, v53
	v_lshl_add_u64 v[64:65], v[64:65], 0, v[4:5]
	s_mov_b32 m0, s84
	v_ashrrev_i32_e32 v5, 31, v3
	s_mov_b64 exec, s[98:99]
	global_load_lds_dwordx4 v[64:65], off nt
	s_mov_b64 exec, s[100:101]
	v_mul_lo_u32 v5, s20, v5
	v_mul_lo_u32 v7, s21, v3
	v_mad_u64_u32 v[64:65], s[24:25], s20, v3, 0
	v_add3_u32 v65, v65, v5, v7
	v_lshl_add_u64 v[64:65], v[64:65], 2, s[22:23]
	v_mov_b32_e32 v7, v1
	v_add_u32_e32 v3, s0, v54
	v_lshl_add_u64 v[64:65], v[64:65], 0, v[6:7]
	s_mov_b32 m0, s79
	v_ashrrev_i32_e32 v5, 31, v3
	s_mov_b64 exec, s[98:99]
	global_load_lds_dwordx4 v[64:65], off nt
	s_mov_b64 exec, s[100:101]
	v_mul_lo_u32 v5, s20, v5
	v_mul_lo_u32 v7, s21, v3
	v_mad_u64_u32 v[64:65], s[24:25], s20, v3, 0
	v_add3_u32 v65, v65, v5, v7
	v_lshl_add_u64 v[64:65], v[64:65], 2, s[22:23]
	v_mov_b32_e32 v9, v1
	v_add_u32_e32 v3, s0, v55
	v_lshl_add_u64 v[64:65], v[64:65], 0, v[8:9]
	s_mov_b32 m0, s78
	v_ashrrev_i32_e32 v5, 31, v3
	s_mov_b64 exec, s[98:99]
	global_load_lds_dwordx4 v[64:65], off nt
	s_mov_b64 exec, s[100:101]
	v_mul_lo_u32 v5, s20, v5
	v_mul_lo_u32 v7, s21, v3
	v_mad_u64_u32 v[64:65], s[24:25], s20, v3, 0
	v_add3_u32 v65, v65, v5, v7
	v_lshl_add_u64 v[64:65], v[64:65], 2, s[22:23]
	v_mov_b32_e32 v11, v1
	v_add_u32_e32 v3, s0, v56
	v_lshl_add_u64 v[64:65], v[64:65], 0, v[10:11]
	s_mov_b32 m0, s77
	v_ashrrev_i32_e32 v5, 31, v3
	s_mov_b64 exec, s[98:99]
	global_load_lds_dwordx4 v[64:65], off nt
	s_mov_b64 exec, s[100:101]
	v_mul_lo_u32 v5, s20, v5
	v_mul_lo_u32 v7, s21, v3
	v_mad_u64_u32 v[64:65], s[24:25], s20, v3, 0
	v_add3_u32 v65, v65, v5, v7
	v_lshl_add_u64 v[64:65], v[64:65], 2, s[22:23]
	v_mov_b32_e32 v13, v1
	v_add_u32_e32 v3, s0, v57
	v_lshl_add_u64 v[64:65], v[64:65], 0, v[12:13]
	s_mov_b32 m0, s29
	v_ashrrev_i32_e32 v5, 31, v3
	s_mov_b64 exec, s[98:99]
	global_load_lds_dwordx4 v[64:65], off nt
	s_mov_b64 exec, s[100:101]
	v_mul_lo_u32 v5, s20, v5
	v_mul_lo_u32 v7, s21, v3
	v_mad_u64_u32 v[64:65], s[20:21], s20, v3, 0
	v_add3_u32 v65, v65, v5, v7
	v_lshl_add_u64 v[64:65], v[64:65], 2, s[22:23]
	v_mov_b32_e32 v15, v1
	v_lshl_add_u64 v[64:65], v[64:65], 0, v[14:15]
	s_add_i32 m0, s28, s61
	s_cmp_lt_i32 s75, s34
	s_mov_b64 exec, s[98:99]
	global_load_lds_dwordx4 v[64:65], off nt
	s_mov_b64 exec, s[100:101]
	s_cselect_b32 s21, s31, s33
	s_add_i32 s21, s21, s75
	s_cmpk_gt_i32 s21, 0x37f
	s_mov_b64 s[26:27], -1
	s_cbranch_scc0 .LBB0_1058
	s_cmpk_gt_u32 s21, 0x47f
	s_cbranch_scc0 .LBB0_1055
	s_cmpk_gt_u32 s21, 0x67f
	s_cbranch_scc0 .LBB0_1052
	s_cmpk_gt_u32 s21, 0x467f
	s_mov_b64 s[22:23], -1
	s_cbranch_scc0 .LBB0_1049
	s_add_i32 s0, s21, 0xffffb980
	s_lshr_b32 s0, s0, 7
	s_lshl_b32 s20, s21, 7
	s_lshl_b32 s22, s21, 4
	s_and_b32 s20, s20, 0x380
	s_and_b32 s28, s22, 0x780
	s_lshl_b64 s[22:23], s[0:1], 22
	s_add_u32 s24, s73, s22
	s_addc_u32 s25, s74, s23
	s_mov_b64 s[22:23], 0

; #define CV_ISSUE(i, buf) do { const ConvJob _j = CV_JOB(i); _Pragma("unroll") for (int _q = 0; _q < 8; ++_q) { const int _row = 2 * (_q * 8 + w) + lrow; const int _g = gp ^ cv_fz(_row); \
;         __builtin_amdgcn_global_load_lds((const unsigned*)(_j.src + (size_t)(_j.k0 + _row) * _j.ld + _j.col0 + _g * 4), (LAS unsigned*)(c.lds + (buf) * 65536 + (_q * 8 + w) * 1024), 16, 0, 2); } } while (0)
; __device__ __forceinline__ void conv_slice(const Ctx& c, int lo0, int n0, int lo1, int n1, int lo2, int n2) {
;     ...
;     CV_ISSUE(0, 0); CV_ISSUE(1, 1);
;     for (int i = 0; i < mine; ++i) {
;         if (i == 0) asm volatile("s_waitcnt vmcnt(8)" ::: "memory"); else if (i == 1) asm volatile("s_waitcnt vmcnt(12)" ::: "memory"); else asm volatile("s_waitcnt vmcnt(16)" ::: "memory");
.LBB0_1269:
	s_add_i32 s98, s84, 2
	s_cmp_le_i32 s98, s76
	s_cselect_b64 s[98:99], exec, 0
	s_mov_b64 s[100:101], exec
	s_cmp_lt_i32 s84, s76
	s_cbranch_scc1 .Lcv_nl_4
	s_waitcnt vmcnt(4)

; __device__ __forceinline__ ConvJob conv_job(const Ctx& c, int t) {
;     ...
;     if (i < CV_IN) { const int kb = i % 16, cb = i / 16; j.src = c.in[4]; j.ld = NIN; j.k0 = kb * 128; j.col0 = cb * 128; j.dst = WSP(bf16, WS_WIN); j.dK = 2048; j.drow0 = cb * 128; return j; }
;     i -= CV_IN;
;     if (i < CV_OUT) { const int kb = i % 16, cb = i / 16; j.src = c.in[8]; j.ld = 2048; j.k0 = kb * 128; j.col0 = cb * 128; j.dst = WSP(bf16, WS_WOUT); j.dK = 2048; j.drow0 = cb * 128; return j; }
;     i -= CV_OUT;
;     if (i < CV_GLU) { const int kb = i % 16, cb = i / 16; j.src = c.in[17]; j.ld = 4096; j.k0 = kb * 128; j.col0 = cb * 128; j.dst = WSP(bf16, WS_WGLU); j.dK = 2048; j.drow0 = cb < 16 ? cb * 256 : (cb - 16) * 256 + 128; return j; }
;     i -= CV_GLU;
;     if (i < CV_GU) { const int kb = i % 16, cb = (i / 16) % 8, gu = (i / 128) % 2, le = i / 256;
;         j.src = (gu ? c.in[23] : c.in[22]) + (size_t)le * 2048 * 1024; j.ld = 1024; j.k0 = kb * 128; j.col0 = cb * 128; j.dst = WSP(bf16, WS_WGU) + (size_t)le * 2048 * 2048; j.dK = 2048; j.drow0 = cb * 256 + gu * 128; return j; }
;     i -= CV_GU;
;     { const int kb = i % 8, cb = (i / 8) % 16, le = i / 128;
;         j.src = c.in[24] + (size_t)le * 1024 * 2048; j.ld = 2048; j.k0 = kb * 128; j.col0 = cb * 128; j.dst = WSP(bf16, WS_WD) + (size_t)le * 2048 * 1024; j.dK = 1024; j.drow0 = cb * 128; return j; }
.LBB0_1305:
	s_ashr_i32 s23, s22, 31
	s_lshl_b64 s[22:23], s[22:23], 2
	v_add_u32_e32 v3, s0, v50
	s_add_u32 s20, s20, s22
	v_ashrrev_i32_e32 v5, 31, v3
	s_addc_u32 s21, s21, s23
	v_mul_lo_u32 v5, s18, v5
	v_mul_lo_u32 v7, s19, v3
	v_mad_u64_u32 v[64:65], s[22:23], s18, v3, 0
	v_add3_u32 v65, v65, v5, v7
	v_lshl_add_u64 v[64:65], v[64:65], 2, s[20:21]
	v_add_u32_e32 v3, s0, v51
	s_mov_b32 m0, s69
	v_lshl_add_u64 v[64:65], v[64:65], 0, v[0:1]
	v_ashrrev_i32_e32 v5, 31, v3
	s_mov_b64 exec, s[98:99]
	global_load_lds_dwordx4 v[64:65], off nt
	s_mov_b64 exec, s[100:101]
	v_mul_lo_u32 v5, s18, v5
	v_mul_lo_u32 v7, s19, v3
	v_mad_u64_u32 v[64:65], s[22:23], s18, v3, 0
	v_add3_u32 v65, v65, v5, v7
	v_lshl_add_u64 v[64:65], v[64:65], 2, s[20:21]
	v_mov_b32_e32 v3, v1
	v_lshl_add_u64 v[64:65], v[64:65], 0, v[2:3]
	v_add_u32_e32 v3, s0, v52
	s_mov_b32 m0, s70
	v_ashrrev_i32_e32 v5, 31, v3
	s_mov_b64 exec, s[98:99]
	global_load_lds_dwordx4 v[64:65], off nt
	s_mov_b64 exec, s[100:101]
	v_mul_lo_u32 v5, s18, v5
	v_mul_lo_u32 v7, s19, v3
	v_mad_u64_u32 v[64:65], s[22:23], s18, v3, 0
	v_add3_u32 v65, v65, v5, v7
	v_lshl_add_u64 v[64:65], v[64:65], 2, s[20:21]
	v_mov_b32_e32 v5, v1
	v_add_u32_e32 v3, s0, v53
	v_lshl_add_u64 v[64:65], v[64:65], 0, v[4:5]
	s_mov_b32 m0, s97
	v_ashrrev_i32_e32 v5, 31, v3
	s_mov_b64 exec, s[98:99]
	global_load_lds_dwordx4 v[64:65], off nt
	s_mov_b64 exec, s[100:101]
	v_mul_lo_u32 v5, s18, v5
	v_mul_lo_u32 v7, s19, v3
	v_mad_u64_u32 v[64:65], s[22:23], s18, v3, 0
	v_add3_u32 v65, v65, v5, v7
	v_lshl_add_u64 v[64:65], v[64:65], 2, s[20:21]
	v_mov_b32_e32 v7, v1
	v_add_u32_e32 v3, s0, v54
	v_lshl_add_u64 v[64:65], v[64:65], 0, v[6:7]
	s_mov_b32 m0, s89
	v_ashrrev_i32_e32 v5, 31, v3
	s_mov_b64 exec, s[98:99]
	global_load_lds_dwordx4 v[64:65], off nt
	s_mov_b64 exec, s[100:101]
	v_mul_lo_u32 v5, s18, v5
	v_mul_lo_u32 v7, s19, v3
	v_mad_u64_u32 v[64:65], s[22:23], s18, v3, 0
	v_add3_u32 v65, v65, v5, v7
	v_lshl_add_u64 v[64:65], v[64:65], 2, s[20:21]
	v_mov_b32_e32 v9, v1
	v_add_u32_e32 v3, s0, v55
	v_lshl_add_u64 v[64:65], v[64:65], 0, v[8:9]
	s_mov_b32 m0, s88
	v_ashrrev_i32_e32 v5, 31, v3
	s_mov_b64 exec, s[98:99]
	global_load_lds_dwordx4 v[64:65], off nt
	s_mov_b64 exec, s[100:101]
	v_mul_lo_u32 v5, s18, v5
	v_mul_lo_u32 v7, s19, v3
	v_mad_u64_u32 v[64:65], s[22:23], s18, v3, 0
	v_add3_u32 v65, v65, v5, v7
	v_lshl_add_u64 v[64:65], v[64:65], 2, s[20:21]
	v_mov_b32_e32 v11, v1
	v_add_u32_e32 v3, s0, v56
	v_lshl_add_u64 v[64:65], v[64:65], 0, v[10:11]
	s_mov_b32 m0, s85
	v_ashrrev_i32_e32 v5, 31, v3
	s_mov_b64 exec, s[98:99]
	global_load_lds_dwordx4 v[64:65], off nt
	s_mov_b64 exec, s[100:101]
	v_mul_lo_u32 v5, s18, v5
	v_mul_lo_u32 v7, s19, v3
	v_mad_u64_u32 v[64:65], s[22:23], s18, v3, 0
	v_add3_u32 v65, v65, v5, v7
	v_lshl_add_u64 v[64:65], v[64:65], 2, s[20:21]
	v_mov_b32_e32 v13, v1
	v_add_u32_e32 v3, s0, v57
	v_lshl_add_u64 v[64:65], v[64:65], 0, v[12:13]
	s_mov_b32 m0, s27
	v_ashrrev_i32_e32 v5, 31, v3
	s_mov_b64 exec, s[98:99]
	global_load_lds_dwordx4 v[64:65], off nt
	s_mov_b64 exec, s[100:101]
	v_mul_lo_u32 v5, s18, v5
	v_mul_lo_u32 v7, s19, v3
	v_mad_u64_u32 v[64:65], s[18:19], s18, v3, 0
	v_add3_u32 v65, v65, v5, v7
	v_lshl_add_u64 v[64:65], v[64:65], 2, s[20:21]
	v_mov_b32_e32 v15, v1
	v_lshl_add_u64 v[64:65], v[64:65], 0, v[14:15]
	s_add_i32 m0, s26, s87
	s_cmp_ge_i32 s79, s42
	s_mov_b64 exec, s[98:99]
	global_load_lds_dwordx4 v[64:65], off nt
	s_mov_b64 exec, s[100:101]
	s_cselect_b32 s19, s49, 0x2680
	s_add_i32 s19, s19, s79
	s_cmpk_gt_i32 s19, 0x37f
	s_mov_b64 s[24:25], -1
	s_cbranch_scc0 .LBB0_1319
	s_cmpk_gt_u32 s19, 0x47f
	s_cbranch_scc0 .LBB0_1316
	s_cmpk_gt_u32 s19, 0x67f
	s_cbranch_scc0 .LBB0_1313
	s_cmpk_gt_u32 s19, 0x467f
	s_mov_b64 s[20:21], -1
	s_cbranch_scc0 .LBB0_1310
	s_add_i32 s0, s19, 0xffffb980
	s_lshr_b32 s0, s0, 7
	s_lshl_b32 s18, s19, 7
	s_lshl_b32 s20, s19, 4
	s_and_b32 s18, s18, 0x380
	s_and_b32 s26, s20, 0x780
	s_lshl_b64 s[20:21], s[0:1], 22
	s_add_u32 s22, s10, s20
	s_addc_u32 s23, s11, s21
	s_mov_b64 s[20:21], 0

; __device__ __forceinline__ ConvJob conv_job(const Ctx& c, int t) {
;     ...
;     if (i < CV_IN) { const int kb = i % 16, cb = i / 16; j.src = c.in[4]; j.ld = NIN; j.k0 = kb * 128; j.col0 = cb * 128; j.dst = WSP(bf16, WS_WIN); j.dK = 2048; j.drow0 = cb * 128; return j; }
;     i -= CV_IN;
;     if (i < CV_OUT) { const int kb = i % 16, cb = i / 16; j.src = c.in[8]; j.ld = 2048; j.k0 = kb * 128; j.col0 = cb * 128; j.dst = WSP(bf16, WS_WOUT); j.dK = 2048; j.drow0 = cb * 128; return j; }
;     i -= CV_OUT;
;     if (i < CV_GLU) { const int kb = i % 16, cb = i / 16; j.src = c.in[17]; j.ld = 4096; j.k0 = kb * 128; j.col0 = cb * 128; j.dst = WSP(bf16, WS_WGLU); j.dK = 2048; j.drow0 = cb < 16 ? cb * 256 : (cb - 16) * 256 + 128; return j; }
;     i -= CV_GLU;
;     if (i < CV_GU) { const int kb = i % 16, cb = (i / 16) % 8, gu = (i / 128) % 2, le = i / 256;
;         j.src = (gu ? c.in[23] : c.in[22]) + (size_t)le * 2048 * 1024; j.ld = 1024; j.k0 = kb * 128; j.col0 = cb * 128; j.dst = WSP(bf16, WS_WGU) + (size_t)le * 2048 * 2048; j.dK = 2048; j.drow0 = cb * 256 + gu * 128; return j; }
;     i -= CV_GU;
;     { const int kb = i % 8, cb = (i / 8) % 16, le = i / 128;
;         j.src = c.in[24] + (size_t)le * 1024 * 2048; j.ld = 2048; j.k0 = kb * 128; j.col0 = cb * 128; j.dst = WSP(bf16, WS_WD) + (size_t)le * 2048 * 1024; j.dK = 1024; j.drow0 = cb * 128; return j; }
.LBB0_1407:
	s_ashr_i32 s23, s22, 31
	s_lshl_b64 s[22:23], s[22:23], 2
	v_add_u32_e32 v3, s0, v50
	s_add_u32 s20, s20, s22
	v_ashrrev_i32_e32 v5, 31, v3
	s_addc_u32 s21, s21, s23
	v_mul_lo_u32 v5, s18, v5
	v_mul_lo_u32 v7, s19, v3
	v_mad_u64_u32 v[64:65], s[22:23], s18, v3, 0
	v_add3_u32 v65, v65, v5, v7
	v_lshl_add_u64 v[64:65], v[64:65], 2, s[20:21]
	v_add_u32_e32 v3, s0, v51
	s_mov_b32 m0, s37
	v_lshl_add_u64 v[64:65], v[64:65], 0, v[0:1]
	v_ashrrev_i32_e32 v5, 31, v3
	s_mov_b64 exec, s[98:99]
	global_load_lds_dwordx4 v[64:65], off nt
	s_mov_b64 exec, s[100:101]
	v_mul_lo_u32 v5, s18, v5
	v_mul_lo_u32 v7, s19, v3
	v_mad_u64_u32 v[64:65], s[22:23], s18, v3, 0
	v_add3_u32 v65, v65, v5, v7
	v_lshl_add_u64 v[64:65], v[64:65], 2, s[20:21]
	v_mov_b32_e32 v3, v1
	v_lshl_add_u64 v[64:65], v[64:65], 0, v[2:3]
	v_add_u32_e32 v3, s0, v52
	s_mov_b32 m0, s36
	v_ashrrev_i32_e32 v5, 31, v3
	s_mov_b64 exec, s[98:99]
	global_load_lds_dwordx4 v[64:65], off nt
	s_mov_b64 exec, s[100:101]
	v_mul_lo_u32 v5, s18, v5
	v_mul_lo_u32 v7, s19, v3
	v_mad_u64_u32 v[64:65], s[22:23], s18, v3, 0
	v_add3_u32 v65, v65, v5, v7
	v_lshl_add_u64 v[64:65], v[64:65], 2, s[20:21]
	v_mov_b32_e32 v5, v1
	v_add_u32_e32 v3, s0, v53
	v_lshl_add_u64 v[64:65], v[64:65], 0, v[4:5]
	s_mov_b32 m0, s84
	v_ashrrev_i32_e32 v5, 31, v3
	s_mov_b64 exec, s[98:99]
	global_load_lds_dwordx4 v[64:65], off nt
	s_mov_b64 exec, s[100:101]
	v_mul_lo_u32 v5, s18, v5
	v_mul_lo_u32 v7, s19, v3
	v_mad_u64_u32 v[64:65], s[22:23], s18, v3, 0
	v_add3_u32 v65, v65, v5, v7
	v_lshl_add_u64 v[64:65], v[64:65], 2, s[20:21]
	v_mov_b32_e32 v7, v1
	v_add_u32_e32 v3, s0, v54
	v_lshl_add_u64 v[64:65], v[64:65], 0, v[6:7]
	s_mov_b32 m0, s79
	v_ashrrev_i32_e32 v5, 31, v3
	s_mov_b64 exec, s[98:99]
	global_load_lds_dwordx4 v[64:65], off nt
	s_mov_b64 exec, s[100:101]
	v_mul_lo_u32 v5, s18, v5
	v_mul_lo_u32 v7, s19, v3
	v_mad_u64_u32 v[64:65], s[22:23], s18, v3, 0
	v_add3_u32 v65, v65, v5, v7
	v_lshl_add_u64 v[64:65], v[64:65], 2, s[20:21]
	v_mov_b32_e32 v9, v1
	v_add_u32_e32 v3, s0, v55
	v_lshl_add_u64 v[64:65], v[64:65], 0, v[8:9]
	s_mov_b32 m0, s78
	v_ashrrev_i32_e32 v5, 31, v3
	s_mov_b64 exec, s[98:99]
	global_load_lds_dwordx4 v[64:65], off nt
	s_mov_b64 exec, s[100:101]
	v_mul_lo_u32 v5, s18, v5
	v_mul_lo_u32 v7, s19, v3
	v_mad_u64_u32 v[64:65], s[22:23], s18, v3, 0
	v_add3_u32 v65, v65, v5, v7
	v_lshl_add_u64 v[64:65], v[64:65], 2, s[20:21]
	v_mov_b32_e32 v11, v1
	v_add_u32_e32 v3, s0, v56
	v_lshl_add_u64 v[64:65], v[64:65], 0, v[10:11]
	s_mov_b32 m0, s77
	v_ashrrev_i32_e32 v5, 31, v3
	s_mov_b64 exec, s[98:99]
	global_load_lds_dwordx4 v[64:65], off nt
	s_mov_b64 exec, s[100:101]
	v_mul_lo_u32 v5, s18, v5
	v_mul_lo_u32 v7, s19, v3
	v_mad_u64_u32 v[64:65], s[22:23], s18, v3, 0
	v_add3_u32 v65, v65, v5, v7
	v_lshl_add_u64 v[64:65], v[64:65], 2, s[20:21]
	v_mov_b32_e32 v13, v1
	v_add_u32_e32 v3, s0, v57
	v_lshl_add_u64 v[64:65], v[64:65], 0, v[12:13]
	s_mov_b32 m0, s27
	v_ashrrev_i32_e32 v5, 31, v3
	s_mov_b64 exec, s[98:99]
	global_load_lds_dwordx4 v[64:65], off nt
	s_mov_b64 exec, s[100:101]
	v_mul_lo_u32 v5, s18, v5
	v_mul_lo_u32 v7, s19, v3
	v_mad_u64_u32 v[64:65], s[18:19], s18, v3, 0
	v_add3_u32 v65, v65, v5, v7
	v_lshl_add_u64 v[64:65], v[64:65], 2, s[20:21]
	v_mov_b32_e32 v15, v1
	v_lshl_add_u64 v[64:65], v[64:65], 0, v[14:15]
	s_add_i32 m0, s26, s61
	s_cmp_lt_i32 s75, s43
	s_mov_b64 exec, s[98:99]
	global_load_lds_dwordx4 v[64:65], off nt
	s_mov_b64 exec, s[100:101]
	s_cselect_b32 s19, s41, s42
	s_add_i32 s19, s19, s75
	s_cmpk_gt_i32 s19, 0x37f
	s_mov_b64 s[24:25], -1
	s_cbranch_scc0 .LBB0_1421
	s_cmpk_gt_u32 s19, 0x47f
	s_cbranch_scc0 .LBB0_1418
	s_cmpk_gt_u32 s19, 0x67f
	s_cbranch_scc0 .LBB0_1415
	s_cmpk_gt_u32 s19, 0x467f
	s_mov_b64 s[20:21], -1
	s_cbranch_scc0 .LBB0_1412
	s_add_i32 s0, s19, 0xffffb980
	s_lshr_b32 s0, s0, 7
	s_lshl_b32 s18, s19, 7
	s_lshl_b32 s20, s19, 4
	s_and_b32 s18, s18, 0x380
	s_and_b32 s26, s20, 0x780
	s_lshl_b64 s[20:21], s[0:1], 22
	s_add_u32 s22, s10, s20
	s_addc_u32 s23, s11, s21
	s_mov_b64 s[20:21], 0

; #define CV_ISSUE(i, buf) do { const ConvJob _j = CV_JOB(i); _Pragma("unroll") for (int _q = 0; _q < 8; ++_q) { const int _row = 2 * (_q * 8 + w) + lrow; const int _g = gp ^ cv_fz(_row); \
;         __builtin_amdgcn_global_load_lds((const unsigned*)(_j.src + (size_t)(_j.k0 + _row) * _j.ld + _j.col0 + _g * 4), (LAS unsigned*)(c.lds + (buf) * 65536 + (_q * 8 + w) * 1024), 16, 0, 2); } } while (0)
; __device__ __forceinline__ void conv_slice(const Ctx& c, int lo0, int n0, int lo1, int n1, int lo2, int n2) {
;     ...
;     CV_ISSUE(0, 0); CV_ISSUE(1, 1);
;     for (int i = 0; i < mine; ++i) {
;         if (i == 0) asm volatile("s_waitcnt vmcnt(8)" ::: "memory"); else if (i == 1) asm volatile("s_waitcnt vmcnt(12)" ::: "memory"); else asm volatile("s_waitcnt vmcnt(16)" ::: "memory");
.LBB0_1910:
	s_add_i32 s98, s75, 2
	s_cmp_le_i32 s98, s62
	s_cselect_b64 s[98:99], exec, 0
	s_mov_b64 s[100:101], exec
	s_cmp_lt_i32 s75, s62
	s_cbranch_scc1 .Lcv_nl_6
	s_waitcnt vmcnt(4)

; __device__ __forceinline__ ConvJob conv_job(const Ctx& c, int t) {
;     ...
;     if (i < CV_IN) { const int kb = i % 16, cb = i / 16; j.src = c.in[4]; j.ld = NIN; j.k0 = kb * 128; j.col0 = cb * 128; j.dst = WSP(bf16, WS_WIN); j.dK = 2048; j.drow0 = cb * 128; return j; }
;     i -= CV_IN;
;     if (i < CV_OUT) { const int kb = i % 16, cb = i / 16; j.src = c.in[8]; j.ld = 2048; j.k0 = kb * 128; j.col0 = cb * 128; j.dst = WSP(bf16, WS_WOUT); j.dK = 2048; j.drow0 = cb * 128; return j; }
;     i -= CV_OUT;
;     if (i < CV_GLU) { const int kb = i % 16, cb = i / 16; j.src = c.in[17]; j.ld = 4096; j.k0 = kb * 128; j.col0 = cb * 128; j.dst = WSP(bf16, WS_WGLU); j.dK = 2048; j.drow0 = cb < 16 ? cb * 256 : (cb - 16) * 256 + 128; return j; }
;     i -= CV_GLU;
;     if (i < CV_GU) { const int kb = i % 16, cb = (i / 16) % 8, gu = (i / 128) % 2, le = i / 256;
;         j.src = (gu ? c.in[23] : c.in[22]) + (size_t)le * 2048 * 1024; j.ld = 1024; j.k0 = kb * 128; j.col0 = cb * 128; j.dst = WSP(bf16, WS_WGU) + (size_t)le * 2048 * 2048; j.dK = 2048; j.drow0 = cb * 256 + gu * 128; return j; }
;     i -= CV_GU;
;     { const int kb = i % 8, cb = (i / 8) % 16, le = i / 128;
;         j.src = c.in[24] + (size_t)le * 1024 * 2048; j.ld = 2048; j.k0 = kb * 128; j.col0 = cb * 128; j.dst = WSP(bf16, WS_WD) + (size_t)le * 2048 * 1024; j.dK = 1024; j.drow0 = cb * 128; return j; }
.LBB0_1946:
	s_ashr_i32 s25, s24, 31
	s_lshl_b64 s[24:25], s[24:25], 2
	v_add_u32_e32 v3, s14, v50
	s_add_u32 s22, s22, s24
	v_ashrrev_i32_e32 v5, 31, v3
	s_addc_u32 s23, s23, s25
	v_mul_lo_u32 v5, s20, v5
	v_mul_lo_u32 v7, s21, v3
	v_mad_u64_u32 v[64:65], s[24:25], s20, v3, 0
	v_add3_u32 v65, v65, v5, v7
	v_lshl_add_u64 v[64:65], v[64:65], 2, s[22:23]
	v_add_u32_e32 v3, s14, v51
	s_mov_b32 m0, s84
	v_lshl_add_u64 v[64:65], v[64:65], 0, v[0:1]
	v_ashrrev_i32_e32 v5, 31, v3
	s_mov_b64 exec, s[98:99]
	global_load_lds_dwordx4 v[64:65], off nt
	s_mov_b64 exec, s[100:101]
	v_mul_lo_u32 v5, s20, v5
	v_mul_lo_u32 v7, s21, v3
	v_mad_u64_u32 v[64:65], s[24:25], s20, v3, 0
	v_add3_u32 v65, v65, v5, v7
	v_lshl_add_u64 v[64:65], v[64:65], 2, s[22:23]
	v_mov_b32_e32 v3, v1
	v_lshl_add_u64 v[64:65], v[64:65], 0, v[2:3]
	v_add_u32_e32 v3, s14, v52
	s_mov_b32 m0, s81
	v_ashrrev_i32_e32 v5, 31, v3
	s_mov_b64 exec, s[98:99]
	global_load_lds_dwordx4 v[64:65], off nt
	s_mov_b64 exec, s[100:101]
	v_mul_lo_u32 v5, s20, v5
	v_mul_lo_u32 v7, s21, v3
	v_mad_u64_u32 v[64:65], s[24:25], s20, v3, 0
	v_add3_u32 v65, v65, v5, v7
	v_lshl_add_u64 v[64:65], v[64:65], 2, s[22:23]
	v_mov_b32_e32 v5, v1
	v_add_u32_e32 v3, s14, v53
	v_lshl_add_u64 v[64:65], v[64:65], 0, v[4:5]
	s_mov_b32 m0, s80
	v_ashrrev_i32_e32 v5, 31, v3
	s_mov_b64 exec, s[98:99]
	global_load_lds_dwordx4 v[64:65], off nt
	s_mov_b64 exec, s[100:101]
	v_mul_lo_u32 v5, s20, v5
	v_mul_lo_u32 v7, s21, v3
	v_mad_u64_u32 v[64:65], s[24:25], s20, v3, 0
	v_add3_u32 v65, v65, v5, v7
	v_lshl_add_u64 v[64:65], v[64:65], 2, s[22:23]
	v_mov_b32_e32 v7, v1
	v_add_u32_e32 v3, s14, v54
	v_lshl_add_u64 v[64:65], v[64:65], 0, v[6:7]
	s_mov_b32 m0, s79
	v_ashrrev_i32_e32 v5, 31, v3
	s_mov_b64 exec, s[98:99]
	global_load_lds_dwordx4 v[64:65], off nt
	s_mov_b64 exec, s[100:101]
	v_mul_lo_u32 v5, s20, v5
	v_mul_lo_u32 v7, s21, v3
	v_mad_u64_u32 v[64:65], s[24:25], s20, v3, 0
	v_add3_u32 v65, v65, v5, v7
	v_lshl_add_u64 v[64:65], v[64:65], 2, s[22:23]
	v_mov_b32_e32 v9, v1
	v_add_u32_e32 v3, s14, v55
	v_lshl_add_u64 v[64:65], v[64:65], 0, v[8:9]
	s_mov_b32 m0, s78
	v_ashrrev_i32_e32 v5, 31, v3
	s_mov_b64 exec, s[98:99]
	global_load_lds_dwordx4 v[64:65], off nt
	s_mov_b64 exec, s[100:101]
	v_mul_lo_u32 v5, s20, v5
	v_mul_lo_u32 v7, s21, v3
	v_mad_u64_u32 v[64:65], s[24:25], s20, v3, 0
	v_add3_u32 v65, v65, v5, v7
	v_lshl_add_u64 v[64:65], v[64:65], 2, s[22:23]
	v_mov_b32_e32 v11, v1
	v_add_u32_e32 v3, s14, v56
	v_lshl_add_u64 v[64:65], v[64:65], 0, v[10:11]
	s_mov_b32 m0, s77
	v_ashrrev_i32_e32 v5, 31, v3
	s_mov_b64 exec, s[98:99]
	global_load_lds_dwordx4 v[64:65], off nt
	s_mov_b64 exec, s[100:101]
	v_mul_lo_u32 v5, s20, v5
	v_mul_lo_u32 v7, s21, v3
	v_mad_u64_u32 v[64:65], s[24:25], s20, v3, 0
	v_add3_u32 v65, v65, v5, v7
	v_lshl_add_u64 v[64:65], v[64:65], 2, s[22:23]
	v_mov_b32_e32 v13, v1
	v_add_u32_e32 v3, s14, v57
	v_lshl_add_u64 v[64:65], v[64:65], 0, v[12:13]
	s_mov_b32 m0, s29
	v_ashrrev_i32_e32 v5, 31, v3
	s_mov_b64 exec, s[98:99]
	global_load_lds_dwordx4 v[64:65], off nt
	s_mov_b64 exec, s[100:101]
	v_mul_lo_u32 v5, s20, v5
	v_mul_lo_u32 v7, s21, v3
	v_mad_u64_u32 v[64:65], s[20:21], s20, v3, 0
	v_add3_u32 v65, v65, v5, v7
	v_lshl_add_u64 v[64:65], v[64:65], 2, s[22:23]
	v_mov_b32_e32 v15, v1
	v_lshl_add_u64 v[64:65], v[64:65], 0, v[14:15]
	s_add_i32 m0, s28, s49
	s_cmpk_lt_i32 s74, 0x1300
	s_mov_b64 exec, s[98:99]
	global_load_lds_dwordx4 v[64:65], off nt
	s_mov_b64 exec, s[100:101]
	s_cselect_b32 s21, s73, 0xffffed00
	s_add_i32 s21, s21, s74
	s_cmpk_gt_i32 s21, 0x37f
	s_mov_b64 s[26:27], -1
	s_cbranch_scc0 .LBB0_1960
	s_cmpk_gt_u32 s21, 0x47f
	s_cbranch_scc0 .LBB0_1957
	s_cmpk_gt_u32 s21, 0x67f
	s_cbranch_scc0 .LBB0_1954
	s_cmpk_gt_u32 s21, 0x467f
	s_mov_b64 s[22:23], -1
	s_cbranch_scc0 .LBB0_1951
	s_add_i32 s14, s21, 0xffffb980
	s_lshr_b32 s14, s14, 7
	s_and_b32 s20, s71, 0x380
	s_and_b32 s28, s69, 0x780
	s_lshl_b64 s[22:23], s[14:15], 22
	s_add_u32 s24, s63, s22
	s_addc_u32 s25, s66, s23
	s_mov_b64 s[22:23], 0

; #define CV_ISSUE(i, buf) do { const ConvJob _j = CV_JOB(i); _Pragma("unroll") for (int _q = 0; _q < 8; ++_q) { const int _row = 2 * (_q * 8 + w) + lrow; const int _g = gp ^ cv_fz(_row); \
;         __builtin_amdgcn_global_load_lds((const unsigned*)(_j.src + (size_t)(_j.k0 + _row) * _j.ld + _j.col0 + _g * 4), (LAS unsigned*)(c.lds + (buf) * 65536 + (_q * 8 + w) * 1024), 16, 0, 2); } } while (0)
; __device__ __forceinline__ void conv_slice(const Ctx& c, int lo0, int n0, int lo1, int n1, int lo2, int n2) {
;     ...
;     CV_ISSUE(0, 0); CV_ISSUE(1, 1);
;     for (int i = 0; i < mine; ++i) {
;         if (i == 0) asm volatile("s_waitcnt vmcnt(8)" ::: "memory"); else if (i == 1) asm volatile("s_waitcnt vmcnt(12)" ::: "memory"); else asm volatile("s_waitcnt vmcnt(16)" ::: "memory");
.LBB0_2234:
	s_add_i32 s98, s78, 2
	s_cmp_le_i32 s98, s72
	s_cselect_b64 s[98:99], exec, 0
	s_mov_b64 s[100:101], exec
	s_cmp_lt_i32 s78, s72
	s_cbranch_scc1 .Lcv_nl_7
	s_waitcnt vmcnt(4)

; __device__ __forceinline__ ConvJob conv_job(const Ctx& c, int t) {
;     ...
;     if (i < CV_IN) { const int kb = i % 16, cb = i / 16; j.src = c.in[4]; j.ld = NIN; j.k0 = kb * 128; j.col0 = cb * 128; j.dst = WSP(bf16, WS_WIN); j.dK = 2048; j.drow0 = cb * 128; return j; }
;     i -= CV_IN;
;     if (i < CV_OUT) { const int kb = i % 16, cb = i / 16; j.src = c.in[8]; j.ld = 2048; j.k0 = kb * 128; j.col0 = cb * 128; j.dst = WSP(bf16, WS_WOUT); j.dK = 2048; j.drow0 = cb * 128; return j; }
;     i -= CV_OUT;
;     if (i < CV_GLU) { const int kb = i % 16, cb = i / 16; j.src = c.in[17]; j.ld = 4096; j.k0 = kb * 128; j.col0 = cb * 128; j.dst = WSP(bf16, WS_WGLU); j.dK = 2048; j.drow0 = cb < 16 ? cb * 256 : (cb - 16) * 256 + 128; return j; }
;     i -= CV_GLU;
;     if (i < CV_GU) { const int kb = i % 16, cb = (i / 16) % 8, gu = (i / 128) % 2, le = i / 256;
;         j.src = (gu ? c.in[23] : c.in[22]) + (size_t)le * 2048 * 1024; j.ld = 1024; j.k0 = kb * 128; j.col0 = cb * 128; j.dst = WSP(bf16, WS_WGU) + (size_t)le * 2048 * 2048; j.dK = 2048; j.drow0 = cb * 256 + gu * 128; return j; }
;     i -= CV_GU;
;     { const int kb = i % 8, cb = (i / 8) % 16, le = i / 128;
;         j.src = c.in[24] + (size_t)le * 1024 * 2048; j.ld = 2048; j.k0 = kb * 128; j.col0 = cb * 128; j.dst = WSP(bf16, WS_WD) + (size_t)le * 2048 * 1024; j.dK = 1024; j.drow0 = cb * 128; return j; }
.LBB0_2270:
	s_ashr_i32 s25, s24, 31
	s_lshl_b64 s[24:25], s[24:25], 2
	v_add_u32_e32 v3, s0, v50
	s_add_u32 s22, s22, s24
	v_ashrrev_i32_e32 v5, 31, v3
	s_addc_u32 s23, s23, s25
	v_mul_lo_u32 v5, s20, v5
	v_mul_lo_u32 v7, s21, v3
	v_mad_u64_u32 v[64:65], s[24:25], s20, v3, 0
	v_add3_u32 v65, v65, v5, v7
	v_lshl_add_u64 v[64:65], v[64:65], 2, s[22:23]
	v_add_u32_e32 v3, s0, v51
	s_mov_b32 m0, s86
	v_lshl_add_u64 v[64:65], v[64:65], 0, v[0:1]
	v_ashrrev_i32_e32 v5, 31, v3
	s_mov_b64 exec, s[98:99]
	global_load_lds_dwordx4 v[64:65], off nt
	s_mov_b64 exec, s[100:101]
	v_mul_lo_u32 v5, s20, v5
	v_mul_lo_u32 v7, s21, v3
	v_mad_u64_u32 v[64:65], s[24:25], s20, v3, 0
	v_add3_u32 v65, v65, v5, v7
	v_lshl_add_u64 v[64:65], v[64:65], 2, s[22:23]
	v_mov_b32_e32 v3, v1
	v_lshl_add_u64 v[64:65], v[64:65], 0, v[2:3]
	v_add_u32_e32 v3, s0, v52
	s_mov_b32 m0, s85
	v_ashrrev_i32_e32 v5, 31, v3
	s_mov_b64 exec, s[98:99]
	global_load_lds_dwordx4 v[64:65], off nt
	s_mov_b64 exec, s[100:101]
	v_mul_lo_u32 v5, s20, v5
	v_mul_lo_u32 v7, s21, v3
	v_mad_u64_u32 v[64:65], s[24:25], s20, v3, 0
	v_add3_u32 v65, v65, v5, v7
	v_lshl_add_u64 v[64:65], v[64:65], 2, s[22:23]
	v_mov_b32_e32 v5, v1
	v_add_u32_e32 v3, s0, v53
	v_lshl_add_u64 v[64:65], v[64:65], 0, v[4:5]
	s_mov_b32 m0, s84
	v_ashrrev_i32_e32 v5, 31, v3
	s_mov_b64 exec, s[98:99]
	global_load_lds_dwordx4 v[64:65], off nt
	s_mov_b64 exec, s[100:101]
	v_mul_lo_u32 v5, s20, v5
	v_mul_lo_u32 v7, s21, v3
	v_mad_u64_u32 v[64:65], s[24:25], s20, v3, 0
	v_add3_u32 v65, v65, v5, v7
	v_lshl_add_u64 v[64:65], v[64:65], 2, s[22:23]
	v_mov_b32_e32 v7, v1
	v_add_u32_e32 v3, s0, v54
	v_lshl_add_u64 v[64:65], v[64:65], 0, v[6:7]
	s_mov_b32 m0, s81
	v_ashrrev_i32_e32 v5, 31, v3
	s_mov_b64 exec, s[98:99]
	global_load_lds_dwordx4 v[64:65], off nt
	s_mov_b64 exec, s[100:101]
	v_mul_lo_u32 v5, s20, v5
	v_mul_lo_u32 v7, s21, v3
	v_mad_u64_u32 v[64:65], s[24:25], s20, v3, 0
	v_add3_u32 v65, v65, v5, v7
	v_lshl_add_u64 v[64:65], v[64:65], 2, s[22:23]
	v_mov_b32_e32 v9, v1
	v_add_u32_e32 v3, s0, v55
	v_lshl_add_u64 v[64:65], v[64:65], 0, v[8:9]
	s_mov_b32 m0, s80
	v_ashrrev_i32_e32 v5, 31, v3
	s_mov_b64 exec, s[98:99]
	global_load_lds_dwordx4 v[64:65], off nt
	s_mov_b64 exec, s[100:101]
	v_mul_lo_u32 v5, s20, v5
	v_mul_lo_u32 v7, s21, v3
	v_mad_u64_u32 v[64:65], s[24:25], s20, v3, 0
	v_add3_u32 v65, v65, v5, v7
	v_lshl_add_u64 v[64:65], v[64:65], 2, s[22:23]
	v_mov_b32_e32 v11, v1
	v_add_u32_e32 v3, s0, v56
	v_lshl_add_u64 v[64:65], v[64:65], 0, v[10:11]
	s_mov_b32 m0, s79
	v_ashrrev_i32_e32 v5, 31, v3
	s_mov_b64 exec, s[98:99]
	global_load_lds_dwordx4 v[64:65], off nt
	s_mov_b64 exec, s[100:101]
	v_mul_lo_u32 v5, s20, v5
	v_mul_lo_u32 v7, s21, v3
	v_mad_u64_u32 v[64:65], s[24:25], s20, v3, 0
	v_add3_u32 v65, v65, v5, v7
	v_lshl_add_u64 v[64:65], v[64:65], 2, s[22:23]
	v_mov_b32_e32 v13, v1
	v_add_u32_e32 v3, s0, v57
	v_lshl_add_u64 v[64:65], v[64:65], 0, v[12:13]
	s_mov_b32 m0, s29
	v_ashrrev_i32_e32 v5, 31, v3
	s_mov_b64 exec, s[98:99]
	global_load_lds_dwordx4 v[64:65], off nt
	s_mov_b64 exec, s[100:101]
	v_mul_lo_u32 v5, s20, v5
	v_mul_lo_u32 v7, s21, v3
	v_mad_u64_u32 v[64:65], s[20:21], s20, v3, 0
	v_add3_u32 v65, v65, v5, v7
	v_lshl_add_u64 v[64:65], v[64:65], 2, s[22:23]
	v_mov_b32_e32 v15, v1
	v_lshl_add_u64 v[64:65], v[64:65], 0, v[14:15]
	s_add_i32 m0, s28, s61
	s_cmp_ge_i32 s77, s33
	s_mov_b64 exec, s[98:99]
	global_load_lds_dwordx4 v[64:65], off nt
	s_mov_b64 exec, s[100:101]
	s_cselect_b32 s21, s38, 0x5680
	s_add_i32 s21, s21, s77
	s_cmpk_gt_i32 s21, 0x37f
	s_mov_b64 s[26:27], -1
	s_cbranch_scc0 .LBB0_2284
	s_cmpk_gt_u32 s21, 0x47f
	s_cbranch_scc0 .LBB0_2281
	s_cmpk_gt_u32 s21, 0x67f
	s_cbranch_scc0 .LBB0_2278
	s_cmpk_gt_u32 s21, 0x467f
	s_mov_b64 s[22:23], -1
	s_cbranch_scc0 .LBB0_2275
	s_add_i32 s0, s21, 0xffffb980
	s_lshr_b32 s0, s0, 7
	s_lshl_b32 s20, s21, 7
	s_lshl_b32 s22, s21, 4
	s_and_b32 s20, s20, 0x380
	s_and_b32 s28, s22, 0x780
	s_lshl_b64 s[22:23], s[0:1], 22
	s_add_u32 s24, s73, s22
	s_addc_u32 s25, s74, s23
	s_mov_b64 s[22:23], 0

; #define CV_ISSUE(i, buf) do { const ConvJob _j = CV_JOB(i); _Pragma("unroll") for (int _q = 0; _q < 8; ++_q) { const int _row = 2 * (_q * 8 + w) + lrow; const int _g = gp ^ cv_fz(_row); \
;         __builtin_amdgcn_global_load_lds((const unsigned*)(_j.src + (size_t)(_j.k0 + _row) * _j.ld + _j.col0 + _g * 4), (LAS unsigned*)(c.lds + (buf) * 65536 + (_q * 8 + w) * 1024), 16, 0, 2); } } while (0)
; __device__ __forceinline__ void conv_slice(const Ctx& c, int lo0, int n0, int lo1, int n1, int lo2, int n2) {
;     ...
;     CV_ISSUE(0, 0); CV_ISSUE(1, 1);
;     for (int i = 0; i < mine; ++i) {
;         if (i == 0) asm volatile("s_waitcnt vmcnt(8)" ::: "memory"); else if (i == 1) asm volatile("s_waitcnt vmcnt(12)" ::: "memory"); else asm volatile("s_waitcnt vmcnt(16)" ::: "memory");
.LBB0_2336:
	s_add_i32 s98, s74, 2
	s_cmp_le_i32 s98, s68
	s_cselect_b64 s[98:99], exec, 0
	s_mov_b64 s[100:101], exec
	s_cmp_lt_i32 s74, s68
	s_cbranch_scc1 .Lcv_nl_8
	s_waitcnt vmcnt(4)

; __device__ __forceinline__ ConvJob conv_job(const Ctx& c, int t) {
;     ...
;     if (i < CV_IN) { const int kb = i % 16, cb = i / 16; j.src = c.in[4]; j.ld = NIN; j.k0 = kb * 128; j.col0 = cb * 128; j.dst = WSP(bf16, WS_WIN); j.dK = 2048; j.drow0 = cb * 128; return j; }
;     i -= CV_IN;
;     if (i < CV_OUT) { const int kb = i % 16, cb = i / 16; j.src = c.in[8]; j.ld = 2048; j.k0 = kb * 128; j.col0 = cb * 128; j.dst = WSP(bf16, WS_WOUT); j.dK = 2048; j.drow0 = cb * 128; return j; }
;     i -= CV_OUT;
;     if (i < CV_GLU) { const int kb = i % 16, cb = i / 16; j.src = c.in[17]; j.ld = 4096; j.k0 = kb * 128; j.col0 = cb * 128; j.dst = WSP(bf16, WS_WGLU); j.dK = 2048; j.drow0 = cb < 16 ? cb * 256 : (cb - 16) * 256 + 128; return j; }
;     i -= CV_GLU;
;     if (i < CV_GU) { const int kb = i % 16, cb = (i / 16) % 8, gu = (i / 128) % 2, le = i / 256;
;         j.src = (gu ? c.in[23] : c.in[22]) + (size_t)le * 2048 * 1024; j.ld = 1024; j.k0 = kb * 128; j.col0 = cb * 128; j.dst = WSP(bf16, WS_WGU) + (size_t)le * 2048 * 2048; j.dK = 2048; j.drow0 = cb * 256 + gu * 128; return j; }
;     i -= CV_GU;
;     { const int kb = i % 8, cb = (i / 8) % 16, le = i / 128;
;         j.src = c.in[24] + (size_t)le * 1024 * 2048; j.ld = 2048; j.k0 = kb * 128; j.col0 = cb * 128; j.dst = WSP(bf16, WS_WD) + (size_t)le * 2048 * 1024; j.dK = 1024; j.drow0 = cb * 128; return j; }
.LBB0_2372:
	s_ashr_i32 s25, s24, 31
	s_lshl_b64 s[24:25], s[24:25], 2
	v_add_u32_e32 v3, s0, v50
	s_add_u32 s22, s22, s24
	v_ashrrev_i32_e32 v5, 31, v3
	s_addc_u32 s23, s23, s25
	v_mul_lo_u32 v5, s20, v5
	v_mul_lo_u32 v7, s21, v3
	v_mad_u64_u32 v[64:65], s[24:25], s20, v3, 0
	v_add3_u32 v65, v65, v5, v7
	v_lshl_add_u64 v[64:65], v[64:65], 2, s[22:23]
	v_add_u32_e32 v3, s0, v51
	s_mov_b32 m0, s80
	v_lshl_add_u64 v[64:65], v[64:65], 0, v[0:1]
	v_ashrrev_i32_e32 v5, 31, v3
	s_mov_b64 exec, s[98:99]
	global_load_lds_dwordx4 v[64:65], off nt
	s_mov_b64 exec, s[100:101]
	v_mul_lo_u32 v5, s20, v5
	v_mul_lo_u32 v7, s21, v3
	v_mad_u64_u32 v[64:65], s[24:25], s20, v3, 0
	v_add3_u32 v65, v65, v5, v7
	v_lshl_add_u64 v[64:65], v[64:65], 2, s[22:23]
	v_mov_b32_e32 v3, v1
	v_lshl_add_u64 v[64:65], v[64:65], 0, v[2:3]
	v_add_u32_e32 v3, s0, v52
	s_mov_b32 m0, s79
	v_ashrrev_i32_e32 v5, 31, v3
	s_mov_b64 exec, s[98:99]
	global_load_lds_dwordx4 v[64:65], off nt
	s_mov_b64 exec, s[100:101]
	v_mul_lo_u32 v5, s20, v5
	v_mul_lo_u32 v7, s21, v3
	v_mad_u64_u32 v[64:65], s[24:25], s20, v3, 0
	v_add3_u32 v65, v65, v5, v7
	v_lshl_add_u64 v[64:65], v[64:65], 2, s[22:23]
	v_mov_b32_e32 v5, v1
	v_add_u32_e32 v3, s0, v53
	v_lshl_add_u64 v[64:65], v[64:65], 0, v[4:5]
	s_mov_b32 m0, s78
	v_ashrrev_i32_e32 v5, 31, v3
	s_mov_b64 exec, s[98:99]
	global_load_lds_dwordx4 v[64:65], off nt
	s_mov_b64 exec, s[100:101]
	v_mul_lo_u32 v5, s20, v5
	v_mul_lo_u32 v7, s21, v3
	v_mad_u64_u32 v[64:65], s[24:25], s20, v3, 0
	v_add3_u32 v65, v65, v5, v7
	v_lshl_add_u64 v[64:65], v[64:65], 2, s[22:23]
	v_mov_b32_e32 v7, v1
	v_add_u32_e32 v3, s0, v54
	v_lshl_add_u64 v[64:65], v[64:65], 0, v[6:7]
	s_mov_b32 m0, s77
	v_ashrrev_i32_e32 v5, 31, v3
	s_mov_b64 exec, s[98:99]
	global_load_lds_dwordx4 v[64:65], off nt
	s_mov_b64 exec, s[100:101]
	v_mul_lo_u32 v5, s20, v5
	v_mul_lo_u32 v7, s21, v3
	v_mad_u64_u32 v[64:65], s[24:25], s20, v3, 0
	v_add3_u32 v65, v65, v5, v7
	v_lshl_add_u64 v[64:65], v[64:65], 2, s[22:23]
	v_mov_b32_e32 v9, v1
	v_add_u32_e32 v3, s0, v55
	v_lshl_add_u64 v[64:65], v[64:65], 0, v[8:9]
	s_mov_b32 m0, s76
	v_ashrrev_i32_e32 v5, 31, v3
	s_mov_b64 exec, s[98:99]
	global_load_lds_dwordx4 v[64:65], off nt
	s_mov_b64 exec, s[100:101]
	v_mul_lo_u32 v5, s20, v5
	v_mul_lo_u32 v7, s21, v3
	v_mad_u64_u32 v[64:65], s[24:25], s20, v3, 0
	v_add3_u32 v65, v65, v5, v7
	v_lshl_add_u64 v[64:65], v[64:65], 2, s[22:23]
	v_mov_b32_e32 v11, v1
	v_add_u32_e32 v3, s0, v56
	v_lshl_add_u64 v[64:65], v[64:65], 0, v[10:11]
	s_mov_b32 m0, s75
	v_ashrrev_i32_e32 v5, 31, v3
	s_mov_b64 exec, s[98:99]
	global_load_lds_dwordx4 v[64:65], off nt
	s_mov_b64 exec, s[100:101]
	v_mul_lo_u32 v5, s20, v5
	v_mul_lo_u32 v7, s21, v3
	v_mad_u64_u32 v[64:65], s[24:25], s20, v3, 0
	v_add3_u32 v65, v65, v5, v7
	v_lshl_add_u64 v[64:65], v[64:65], 2, s[22:23]
	v_mov_b32_e32 v13, v1
	v_add_u32_e32 v3, s0, v57
	v_lshl_add_u64 v[64:65], v[64:65], 0, v[12:13]
	s_mov_b32 m0, s29
	v_ashrrev_i32_e32 v5, 31, v3
	s_mov_b64 exec, s[98:99]
	global_load_lds_dwordx4 v[64:65], off nt
	s_mov_b64 exec, s[100:101]
	v_mul_lo_u32 v5, s20, v5
	v_mul_lo_u32 v7, s21, v3
	v_mad_u64_u32 v[64:65], s[20:21], s20, v3, 0
	v_add3_u32 v65, v65, v5, v7
	v_lshl_add_u64 v[64:65], v[64:65], 2, s[22:23]
	v_mov_b32_e32 v15, v1
	v_lshl_add_u64 v[64:65], v[64:65], 0, v[14:15]
	s_add_i32 m0, s28, s53
	s_cmp_lt_i32 s73, s34
	s_mov_b64 exec, s[98:99]
	global_load_lds_dwordx4 v[64:65], off nt
	s_mov_b64 exec, s[100:101]
	s_cselect_b32 s21, s31, s33
	s_add_i32 s21, s21, s73
	s_cmpk_gt_i32 s21, 0x37f
	s_mov_b64 s[26:27], -1
	s_cbranch_scc0 .LBB0_2386
	s_cmpk_gt_u32 s21, 0x47f
	s_cbranch_scc0 .LBB0_2383
	s_cmpk_gt_u32 s21, 0x67f
	s_cbranch_scc0 .LBB0_2380
	s_cmpk_gt_u32 s21, 0x467f
	s_mov_b64 s[22:23], -1
	s_cbranch_scc0 .LBB0_2377
	s_add_i32 s0, s21, 0xffffb980
	s_lshr_b32 s0, s0, 7
	s_lshl_b32 s20, s21, 7
	s_lshl_b32 s22, s21, 4
	s_and_b32 s20, s20, 0x380
	s_and_b32 s28, s22, 0x780
	s_lshl_b64 s[22:23], s[0:1], 22
	s_add_u32 s24, s69, s22
	s_addc_u32 s25, s70, s23
	s_mov_b64 s[22:23], 0

; __global__ void __launch_bounds__(NTHR, 2) mk_fwd(Args args) {
	.amdhsa_kernel _Z6mk_fwd4Args
		.amdhsa_group_segment_fixed_size 0
		.amdhsa_private_segment_fixed_size 0
		.amdhsa_kernarg_size 480
		.amdhsa_user_sgpr_count 2
		.amdhsa_user_sgpr_dispatch_ptr 0
		.amdhsa_user_sgpr_queue_ptr 0
		.amdhsa_user_sgpr_kernarg_segment_ptr 1
		.amdhsa_user_sgpr_dispatch_id 0
		.amdhsa_user_sgpr_kernarg_preload_length 0
		.amdhsa_user_sgpr_kernarg_preload_offset 0
		.amdhsa_user_sgpr_private_segment_size 0
		.amdhsa_uses_dynamic_stack 0
		.amdhsa_enable_private_segment 0
		.amdhsa_system_sgpr_workgroup_id_x 1
		.amdhsa_system_sgpr_workgroup_id_y 0
		.amdhsa_system_sgpr_workgroup_id_z 0
		.amdhsa_system_sgpr_workgroup_info 0
		.amdhsa_system_vgpr_workitem_id 0
		.amdhsa_next_free_vgpr 256
		.amdhsa_next_free_sgpr 102
		.amdhsa_accum_offset 256
		.amdhsa_reserve_vcc 1
		.amdhsa_float_round_mode_32 0
		.amdhsa_float_round_mode_16_64 0
		.amdhsa_float_denorm_mode_32 3
		.amdhsa_float_denorm_mode_16_64 3
		.amdhsa_dx10_clamp 1
		.amdhsa_ieee_mode 1
		.amdhsa_fp16_overflow 0
		.amdhsa_tg_split 0
		.amdhsa_exception_fp_ieee_invalid_op 0
		.amdhsa_exception_fp_denorm_src 0
		.amdhsa_exception_fp_ieee_div_zero 0
		.amdhsa_exception_fp_ieee_overflow 0
		.amdhsa_exception_fp_ieee_underflow 0
		.amdhsa_exception_fp_ieee_inexact 0
		.amdhsa_exception_int_div_zero 0
	.end_amdhsa_kernel

; __global__ void __launch_bounds__(NTHR, 2) mk_fwd(Args args) {
amdhsa.kernels:
  - .agpr_count:     0
    .args:
      - .offset:         0
        .size:           224
        .value_kind:     by_value
      - .offset:         224
        .size:           4
        .value_kind:     hidden_block_count_x
      - .offset:         228
        .size:           4
        .value_kind:     hidden_block_count_y
      - .offset:         232
        .size:           4
        .value_kind:     hidden_block_count_z
      - .offset:         236
        .size:           2
        .value_kind:     hidden_group_size_x
      - .offset:         238
        .size:           2
        .value_kind:     hidden_group_size_y
      - .offset:         240
        .size:           2
        .value_kind:     hidden_group_size_z
      - .offset:         242
        .size:           2
        .value_kind:     hidden_remainder_x
      - .offset:         244
        .size:           2
        .value_kind:     hidden_remainder_y
      - .offset:         246
        .size:           2
        .value_kind:     hidden_remainder_z
      - .offset:         264
        .size:           8
        .value_kind:     hidden_global_offset_x
      - .offset:         272
        .size:           8
        .value_kind:     hidden_global_offset_y
      - .offset:         280
        .size:           8
        .value_kind:     hidden_global_offset_z
      - .offset:         288
        .size:           2
        .value_kind:     hidden_grid_dims
      - .offset:         344
        .size:           4
        .value_kind:     hidden_dynamic_lds_size
    .group_segment_fixed_size: 0
    .kernarg_segment_align: 8
    .kernarg_segment_size: 480
    .language:       OpenCL C
    .language_version:
      - 2
      - 0
    .max_flat_workgroup_size: 512
    .name:           _Z6mk_fwd4Args
    .private_segment_fixed_size: 0
    .sgpr_count:     108
    .sgpr_spill_count: 105
    .symbol:         _Z6mk_fwd4Args.kd
    .uniform_work_group_size: 1
    .uses_dynamic_stack: false
    .vgpr_count:     256
    .vgpr_spill_count: 0
    .wavefront_size: 64
